# conv_a HG row staging: six 16-B loads issued together, one vmcnt(0), six ds_write_b128 (was a six-trip load->wait->write loop); on top of v104
# baseline (speedup 1.0000x reference)
; #define GAS __attribute__((address_space(1)))
; #define LAS __attribute__((address_space(3)))
; __device__ __forceinline__ void conv_a_unit(Frame& F, const bf16* HG, bf16* MIX, const float* dw, const float* dwb, const float* lng, const float* lnb, int unit) {
;     ...
;     for (int ch = tid; ch < 94 * 32; ch += NWAVES * 64) { const int rr = ch >> 5, c16 = ch & 31; const int t = t0 - 30 + rr;
;         v4u v = (v4u){0u, 0u, 0u, 0u}; if (t >= 0) v = *(const GAS v4u*)(HG + (size_t)(row0 - 30 + rr) * 256 + c16 * 8);
;         *(LAS v4u*)(hb + rr * 256 + c16 * 8) = v; }
.LBB0_942:
	s_and_saveexec_b64 s[4:5], s[40:41]
	s_cbranch_execz .LBB0_947
	s_bfe_i32 s7, s18, 0x10019
	s_lshl_b32 s6, s18, 6
	s_lshr_b32 s7, s7, 19
	s_add_i32 s7, s6, s7
	s_and_b32 s7, s7, 0xffffe000
	s_sub_i32 s7, s7, s6
	s_or_b32 s19, s7, 29
	s_sub_i32 s20, s6, 30
	v_ashrrev_i32_e32 v124, 5, v1
	v_add_u32_e32 v125, 16, v124
	v_add_u32_e32 v126, 32, v124
	v_add_u32_e32 v127, 48, v124
	v_add_u32_e32 v128, 64, v124
	v_add_u32_e32 v129, 0x50, v124
	v_mov_b32_e32 v100, 0
	v_mov_b32_e32 v101, 0
	v_mov_b32_e32 v102, 0
	v_mov_b32_e32 v103, 0
	v_mov_b32_e32 v104, 0
	v_mov_b32_e32 v105, 0
	v_mov_b32_e32 v106, 0
	v_mov_b32_e32 v107, 0
	v_mov_b32_e32 v108, 0
	v_mov_b32_e32 v109, 0
	v_mov_b32_e32 v110, 0
	v_mov_b32_e32 v111, 0
	v_mov_b32_e32 v112, 0
	v_mov_b32_e32 v113, 0
	v_mov_b32_e32 v114, 0
	v_mov_b32_e32 v115, 0
	v_mov_b32_e32 v116, 0
	v_mov_b32_e32 v117, 0
	v_mov_b32_e32 v118, 0
	v_mov_b32_e32 v119, 0
	v_mov_b32_e32 v120, 0
	v_mov_b32_e32 v121, 0
	v_mov_b32_e32 v122, 0
	v_mov_b32_e32 v123, 0
	v_cmp_lt_i32_e32 vcc, s19, v124
	s_and_saveexec_b64 s[8:9], vcc
	v_add_u32_e32 v130, s20, v124
	v_ashrrev_i32_e32 v131, 31, v130
	v_lshlrev_b64 v[130:131], 9, v[130:131]
	v_lshl_add_u64 v[130:131], v[12:13], 0, v[130:131]
	global_load_dwordx4 v[100:103], v[130:131], off
	s_or_b64 exec, exec, s[8:9]
	v_cmp_lt_i32_e32 vcc, s19, v125
	s_and_saveexec_b64 s[8:9], vcc
	v_add_u32_e32 v130, s20, v125
	v_ashrrev_i32_e32 v131, 31, v130
	v_lshlrev_b64 v[130:131], 9, v[130:131]
	v_lshl_add_u64 v[130:131], v[12:13], 0, v[130:131]
	global_load_dwordx4 v[104:107], v[130:131], off
	s_or_b64 exec, exec, s[8:9]
	v_cmp_lt_i32_e32 vcc, s19, v126
	s_and_saveexec_b64 s[8:9], vcc
	v_add_u32_e32 v130, s20, v126
	v_ashrrev_i32_e32 v131, 31, v130
	v_lshlrev_b64 v[130:131], 9, v[130:131]
	v_lshl_add_u64 v[130:131], v[12:13], 0, v[130:131]
	global_load_dwordx4 v[108:111], v[130:131], off
	s_or_b64 exec, exec, s[8:9]
	v_cmp_lt_i32_e32 vcc, s19, v127
	s_and_saveexec_b64 s[8:9], vcc
	v_add_u32_e32 v130, s20, v127
	v_ashrrev_i32_e32 v131, 31, v130
	v_lshlrev_b64 v[130:131], 9, v[130:131]
	v_lshl_add_u64 v[130:131], v[12:13], 0, v[130:131]
	global_load_dwordx4 v[112:115], v[130:131], off
	s_or_b64 exec, exec, s[8:9]
	v_cmp_lt_i32_e32 vcc, s19, v128
	s_and_saveexec_b64 s[8:9], vcc
	v_add_u32_e32 v130, s20, v128
	v_ashrrev_i32_e32 v131, 31, v130
	v_lshlrev_b64 v[130:131], 9, v[130:131]
	v_lshl_add_u64 v[130:131], v[12:13], 0, v[130:131]
	global_load_dwordx4 v[116:119], v[130:131], off
	s_or_b64 exec, exec, s[8:9]
	v_cmp_gt_u32_e32 vcc, 0x1c0, v1
	s_and_saveexec_b64 s[6:7], vcc
	v_cmp_lt_i32_e32 vcc, s19, v129
	s_and_saveexec_b64 s[8:9], vcc
	v_add_u32_e32 v130, s20, v129
	v_ashrrev_i32_e32 v131, 31, v130
	v_lshlrev_b64 v[130:131], 9, v[130:131]
	v_lshl_add_u64 v[130:131], v[12:13], 0, v[130:131]
	global_load_dwordx4 v[120:123], v[130:131], off
	s_or_b64 exec, exec, s[8:9]
	s_or_b64 exec, exec, s[6:7]
	s_waitcnt vmcnt(0)
	v_lshl_add_u32 v130, v124, 9, v82
	ds_write_b128 v130, v[100:103]
	v_lshl_add_u32 v130, v125, 9, v82
	ds_write_b128 v130, v[104:107]
	v_lshl_add_u32 v130, v126, 9, v82
	ds_write_b128 v130, v[108:111]
	v_lshl_add_u32 v130, v127, 9, v82
	ds_write_b128 v130, v[112:115]
	v_lshl_add_u32 v130, v128, 9, v82
	ds_write_b128 v130, v[116:119]
	v_cmp_gt_u32_e32 vcc, 0x1c0, v1
	s_and_saveexec_b64 s[6:7], vcc
	v_lshl_add_u32 v130, v129, 9, v82
	ds_write_b128 v130, v[120:123]
	s_or_b64 exec, exec, s[6:7]
